# v039 + compiler pads (s_nop 0 after the inline-asm waits) dropped from the remaining attention MFMA segments
# baseline (speedup 1.0000x reference)
; #define SBAR() __builtin_amdgcn_sched_barrier(0)
; __device__ __forceinline__ int kg(int row) { return (row >> 1) & 7; }
; __device__ __forceinline__ int v_rd_base(int lane) { return ((lane & 3) << 3) | (((lane >> 2) & 3) << 6) | (((lane >> 4) & 1) << 5) | (((lane >> 5) & 1) << 8); }
; #define BAR_ALL() asm volatile("s_waitcnt lgkmcnt(0)\n\ts_barrier" ::: "memory")
; #define LWN1(a) do { if constexpr (NW == 0) LW1(0, a); else if constexpr (NW == 1) LW1(1, a); else if constexpr (NW == 2) LW1(2, a); else if constexpr (NW == 3) LW1(3, a); else if constexpr (NW == 4) LW1(4, a); else if constexpr (NW == 5) LW1(5, a); else LW1(6, a); } while (0)
; #define DMA_K(tile, b) DMA_KP(Kh, tile, b)
; #define DMA_V(tile, b) DMA_VP(Vh, tile, b)
; template <int DQK, bool HASQK, bool HASPV, int J> ...
;     ...
;     if constexpr (J < NS) {
;         constexpr int rd1 = (J + 1 < NS) ? ((J + 1 < NQS) ? 1 : 2) : 0, rd2 = (J + 2 < NS) ? ((J + 2 < NQS) ? 1 : 2) : 0, rd3 = (J + 3 < NS) ? ((J + 3 < NQS) ? 1 : 2) : 0, NW = rd1 + rd2 + rd3;
;     ...
;         if constexpr (J < NQS) { constexpr int d0 = J >> 1, h = J & 1;
;             LWN1(kf[d0][h]); SBAR();
;             if constexpr (h == 0) p0 = __builtin_amdgcn_mfma_f32_32x32x16_bf16(kf[d0][0], qr[d0], (d0 == 0) ? negm : p0, 0, 0, 0);
;             else p1 = __builtin_amdgcn_mfma_f32_32x32x16_bf16(kf[d0][1], qr[d0], (d0 == 0) ? negm : p1, 0, 0, 0);
;         } else { constexpr int q = J - NQS, g = q >> 2, d = q & 3;
;             LWN2(vf[g][2 * d], vf[g][2 * d + 1]); SBAR();
;             o[d] = __builtin_amdgcn_mfma_f32_32x32x16_bf16(pa[g], (bf16x8){vf[g][2 * d][0], vf[g][2 * d][1], vf[g][2 * d][2], vf[g][2 * d][3], vf[g][2 * d + 1][0], vf[g][2 * d + 1][1], vf[g][2 * d + 1][2], vf[g][2 * d + 1][3]}, o[d], 0, 0, 0);
;         }
;     ...
;     const int vb0 = (int)(uintptr_t)V_lds + v_rd_base(lane);
;     int ka[4];
; #pragma unroll
;     for (int b = 0; b < 4; ++b) ka[b] = (int)(uintptr_t)lds + r32 * RB + ((b * 32 + hi * 16) ^ (kg(r32) << 4));
;     f32x16 p0, p1; bf16x8 pa0, pa1, pa2, pa3;
;     asm volatile("s_waitcnt vmcnt(0)" ::: "memory"); BAR_ALL();
;     if (ATT_SKEW && g == 1) BAR_ALL();
;     ...
;     int ci = 0;
;     if (DMA_M) { DMA_K(2, 2); DMA_V(1, 1); }
;     SEG_M(true, false, 0, 0); BAR_ALL();
.LBB0_602:
	v_lshlrev_b32_e32 v26, 3, v200
	v_and_b32_e32 v23, 0xc0, v23
	s_cmp_lg_u32 0, -1
	v_and_or_b32 v23, v26, 24, v23
	v_and_b32_e32 v24, 32, v24
	v_and_b32_e32 v27, 0x100, v26
	s_cselect_b32 s10, 0, 0
	v_or3_b32 v23, v23, v24, v27
	v_mov_b32_e32 v24, s10
	s_movk_i32 s11, 0x180
	v_lshlrev_b32_e32 v177, 4, v25
	v_mad_u32_u24 v24, v22, s11, v24
	v_and_b32_e32 v25, 0x70, v26
	v_add_u32_e32 v26, 32, v177
	v_xad_u32 v187, v26, v25, v24
	v_add_u32_e32 v26, 64, v177
	v_xad_u32 v205, v26, v25, v24
	v_add_u32_e32 v26, 0x60, v177
	v_xad_u32 v185, v177, v25, v24
	v_xad_u32 v206, v26, v25, v24
	ds_read_b128 v[24:27], v185 offset:0
	ds_read_b128 v[28:31], v185 offset:0x3000
	ds_read_b128 v[32:35], v187 offset:0
	ds_read_b128 v[36:39], v187 offset:0x3000
	s_add_i32 s10, s10, 0x12000
	s_mov_b32 s26, 0
	v_add_u32_e32 v202, s10, v23
	v_mov_b64_e32 v[94:95], v[14:15]
	v_mov_b64_e32 v[92:93], v[12:13]
	v_mov_b64_e32 v[90:91], v[10:11]
	v_mov_b64_e32 v[88:89], v[8:9]
	v_mov_b64_e32 v[86:87], v[6:7]
	v_mov_b64_e32 v[84:85], v[4:5]
	v_mov_b64_e32 v[82:83], v[2:3]
	v_mov_b64_e32 v[80:81], v[0:1]
	s_waitcnt lgkmcnt(3)
	s_waitcnt vmcnt(0)
	s_nop 0
	v_mfma_f32_32x32x16_bf16 v[96:111], v[24:27], v[112:115], v[80:95]
	ds_read_b128 v[24:27], v205 offset:0
	s_waitcnt lgkmcnt(3)
	v_mfma_f32_32x32x16_bf16 v[80:95], v[28:31], v[112:115], v[80:95]
	ds_read_b128 v[28:31], v205 offset:0x3000
	s_waitcnt lgkmcnt(3)
	v_mfma_f32_32x32x16_bf16 v[96:111], v[32:35], v[116:119], v[96:111]
	ds_read_b128 v[32:35], v206 offset:0
	s_waitcnt lgkmcnt(3)
	v_mfma_f32_32x32x16_bf16 v[80:95], v[36:39], v[116:119], v[80:95]
	ds_read_b128 v[36:39], v206 offset:0x3000
	s_waitcnt lgkmcnt(3)
	v_mfma_f32_32x32x16_bf16 v[96:111], v[24:27], v[120:123], v[96:111]
	ds_read_b128 v[24:27], v185 offset:0x80
	s_waitcnt lgkmcnt(3)
	v_mfma_f32_32x32x16_bf16 v[80:95], v[28:31], v[120:123], v[80:95]
	ds_read_b128 v[28:31], v185 offset:0x3080
	s_waitcnt lgkmcnt(3)
	v_mfma_f32_32x32x16_bf16 v[96:111], v[32:35], v[124:127], v[96:111]
	ds_read_b128 v[32:35], v187 offset:0x80
	s_waitcnt lgkmcnt(3)
	v_mfma_f32_32x32x16_bf16 v[80:95], v[36:39], v[124:127], v[80:95]
	ds_read_b128 v[36:39], v187 offset:0x3080
	s_waitcnt lgkmcnt(3)
	v_mfma_f32_32x32x16_bf16 v[96:111], v[24:27], v[128:131], v[96:111]
	ds_read_b128 v[24:27], v205 offset:0x80
	s_waitcnt lgkmcnt(3)
	v_mfma_f32_32x32x16_bf16 v[80:95], v[28:31], v[128:131], v[80:95]
	ds_read_b128 v[28:31], v205 offset:0x3080
	s_waitcnt lgkmcnt(3)
	v_mfma_f32_32x32x16_bf16 v[96:111], v[32:35], v[132:135], v[96:111]
	ds_read_b128 v[32:35], v206 offset:0x80
	s_waitcnt lgkmcnt(3)
	v_mfma_f32_32x32x16_bf16 v[80:95], v[36:39], v[132:135], v[80:95]
	ds_read_b128 v[36:39], v206 offset:0x3080
	s_waitcnt lgkmcnt(3)
	v_mfma_f32_32x32x16_bf16 v[96:111], v[24:27], v[136:139], v[96:111]
	ds_read_b128 v[24:27], v185 offset:0x100
	s_waitcnt lgkmcnt(3)
	v_mfma_f32_32x32x16_bf16 v[80:95], v[28:31], v[136:139], v[80:95]
	ds_read_b128 v[28:31], v185 offset:0x3100
	s_waitcnt lgkmcnt(3)
	v_mfma_f32_32x32x16_bf16 v[96:111], v[32:35], v[140:143], v[96:111]
	ds_read_b128 v[32:35], v187 offset:0x100
	s_waitcnt lgkmcnt(3)
	v_mfma_f32_32x32x16_bf16 v[80:95], v[36:39], v[140:143], v[80:95]
	ds_read_b128 v[36:39], v187 offset:0x3100
	s_waitcnt lgkmcnt(3)
	v_mfma_f32_32x32x16_bf16 v[96:111], v[24:27], v[144:147], v[96:111]
	ds_read_b128 v[24:27], v205 offset:0x100
	s_waitcnt lgkmcnt(3)
	v_mfma_f32_32x32x16_bf16 v[80:95], v[28:31], v[144:147], v[80:95]
	ds_read_b128 v[28:31], v205 offset:0x3100
	s_waitcnt lgkmcnt(3)
	v_mfma_f32_32x32x16_bf16 v[96:111], v[32:35], v[148:151], v[96:111]
	ds_read_b128 v[32:35], v206 offset:0x100
	s_waitcnt lgkmcnt(3)
	v_mfma_f32_32x32x16_bf16 v[80:95], v[36:39], v[148:151], v[80:95]
	ds_read_b128 v[36:39], v206 offset:0x3100
	s_waitcnt lgkmcnt(3)
	v_mfma_f32_32x32x16_bf16 v[96:111], v[24:27], v[152:155], v[96:111]
	s_waitcnt lgkmcnt(2)
	v_mfma_f32_32x32x16_bf16 v[80:95], v[28:31], v[152:155], v[80:95]
	s_waitcnt lgkmcnt(1)
	v_mfma_f32_32x32x16_bf16 v[96:111], v[32:35], v[156:159], v[96:111]
	s_waitcnt lgkmcnt(0)
	v_mfma_f32_32x32x16_bf16 v[80:95], v[36:39], v[156:159], v[80:95]
	s_mul_i32 s53, s46, 0x180
	s_add_u32 s52, s52, s53
	s_addc_u32 s47, s47, 0
	s_add_u32 s52, s79, s52
	s_addc_u32 s53, s80, s47
	s_lshl_b32 s46, s46, 8
	s_add_u32 s44, s44, s46
	v_lshlrev_b32_e32 v20, 2, v20
	v_lshlrev_b32_e32 v17, 2, v17
	s_addc_u32 s45, s45, 0
	v_and_b32_e32 v20, 0xffffe000, v20
	v_lshlrev_b32_e32 v18, 10, v18
	v_and_b32_e32 v17, 0xffffe000, v17
	v_or3_b32 v20, v20, v18, v21
	s_add_u32 s44, s81, s44
	v_or3_b32 v17, v17, v18, v19
	s_waitcnt lgkmcnt(0)
	s_barrier
	v_add_u32_e32 v20, v20, v16
	v_mov_b32_e32 v21, v179
	s_addc_u32 s45, s82, s45
	v_add_u32_e32 v16, v17, v16
	v_mov_b32_e32 v17, v179
	v_mov_b32_e32 v64, v179
	v_mov_b32_e32 v65, v179
	v_lshl_add_u32 v201, v22, 2, s67
	v_mov_b32_e32 v181, v179
	v_mov_b32_e32 v183, v179
	v_lshl_add_u64 v[194:195], s[44:45], 0, v[20:21]
	v_lshl_add_u64 v[196:197], s[44:45], 0, v[16:17]
	v_mov_b32_e32 v66, v179
	v_mov_b32_e32 v67, v179
	v_mov_b32_e32 v68, v179
	v_mov_b32_e32 v69, v179
	v_mov_b32_e32 v70, v179
	v_mov_b32_e32 v71, v179
	v_mov_b32_e32 v72, v179
	v_mov_b32_e32 v73, v179
	v_mov_b32_e32 v74, v179
	v_mov_b32_e32 v75, v179
	v_mov_b32_e32 v76, v179
	v_mov_b32_e32 v77, v179
	v_mov_b32_e32 v78, v179
	v_mov_b32_e32 v79, v179
	v_mov_b64_e32 v[48:49], v[64:65]
	v_mov_b64_e32 v[32:33], v[64:65]
	v_mov_b64_e32 v[16:17], v[64:65]
	v_cmp_gt_u32_e64 s[10:11], 32, v200
	v_lshl_add_u64 v[188:189], s[52:53], 0, v[178:179]
	v_lshl_add_u64 v[190:191], s[52:53], 0, v[180:181]
	v_lshl_add_u64 v[192:193], s[52:53], 0, v[182:183]
	v_mov_b32_e32 v204, 0
	s_mov_b64 s[44:45], 0
	v_mov_b64_e32 v[50:51], v[66:67]
	v_mov_b64_e32 v[52:53], v[68:69]
	v_mov_b64_e32 v[54:55], v[70:71]
	v_mov_b64_e32 v[56:57], v[72:73]
	v_mov_b64_e32 v[58:59], v[74:75]
	v_mov_b64_e32 v[60:61], v[76:77]
	v_mov_b64_e32 v[62:63], v[78:79]
	v_mov_b64_e32 v[34:35], v[66:67]
	v_mov_b64_e32 v[36:37], v[68:69]
	v_mov_b64_e32 v[38:39], v[70:71]
	v_mov_b64_e32 v[40:41], v[72:73]
	v_mov_b64_e32 v[42:43], v[74:75]
	v_mov_b64_e32 v[44:45], v[76:77]
	v_mov_b64_e32 v[46:47], v[78:79]
	v_mov_b64_e32 v[18:19], v[66:67]
	v_mov_b64_e32 v[20:21], v[68:69]
	v_mov_b64_e32 v[22:23], v[70:71]
	v_mov_b64_e32 v[24:25], v[72:73]
	v_mov_b64_e32 v[26:27], v[74:75]
	v_mov_b64_e32 v[28:29], v[76:77]
	v_mov_b64_e32 v[30:31], v[78:79]
	v_mov_b32_e32 v203, 0
	s_branch .LBB0_606

; #define SBAR() __builtin_amdgcn_sched_barrier(0)
; #define LWN1(a) do { if constexpr (NW == 0) LW1(0, a); else if constexpr (NW == 1) LW1(1, a); else if constexpr (NW == 2) LW1(2, a); else if constexpr (NW == 3) LW1(3, a); else if constexpr (NW == 4) LW1(4, a); else if constexpr (NW == 5) LW1(5, a); else LW1(6, a); } while (0)
; #define LWN2(a, b) do { if constexpr (NW == 0) LW2(0, a, b); else if constexpr (NW == 1) LW2(1, a, b); else if constexpr (NW == 2) LW2(2, a, b); else if constexpr (NW == 3) LW2(3, a, b); else if constexpr (NW == 4) LW2(4, a, b); else if constexpr (NW == 5) LW2(5, a, b); else LW2(6, a, b); } while (0)
; template <int DQK, bool HASQK, bool HASPV, int J> ...
;     constexpr int NQS = HASQK ? 2 * (DQK / 16) : 0, NS = NQS + (HASPV ? 16 : 0);
;     if constexpr (J < NS) {
;         constexpr int rd1 = (J + 1 < NS) ? ((J + 1 < NQS) ? 1 : 2) : 0, rd2 = (J + 2 < NS) ? ((J + 2 < NQS) ? 1 : 2) : 0, rd3 = (J + 3 < NS) ? ((J + 3 < NQS) ? 1 : 2) : 0, NW = rd1 + rd2 + rd3;
;     ...
;         if constexpr (J < NQS) { constexpr int d0 = J >> 1, h = J & 1;
;             LWN1(kf[d0][h]); SBAR();
;             if constexpr (h == 0) p0 = __builtin_amdgcn_mfma_f32_32x32x16_bf16(kf[d0][0], qr[d0], (d0 == 0) ? negm : p0, 0, 0, 0);
;             else p1 = __builtin_amdgcn_mfma_f32_32x32x16_bf16(kf[d0][1], qr[d0], (d0 == 0) ? negm : p1, 0, 0, 0);
;         } else { constexpr int q = J - NQS, g = q >> 2, d = q & 3;
;             LWN2(vf[g][2 * d], vf[g][2 * d + 1]); SBAR();
;             o[d] = __builtin_amdgcn_mfma_f32_32x32x16_bf16(pa[g], (bf16x8){vf[g][2 * d][0], vf[g][2 * d][1], vf[g][2 * d][2], vf[g][2 * d][3], vf[g][2 * d + 1][0], vf[g][2 * d + 1][1], vf[g][2 * d + 1][2], vf[g][2 * d + 1][3]}, o[d], 0, 0, 0);
;         }
;     ...
;         SBAR();
;         slot_read<DQK, HASQK, HASPV, J + 4>(kf, vf, ka_, vb_);
;         SBAR();
;         slot_run<DQK, HASQK, HASPV, J + 1>(kf, vf, ka_, vb_, qr, p0, p1, negm, o, pa);
.LBB0_631:
	s_add_i32 s34, s26, 1
	s_cmp_lg_u32 s26, 2
	s_cselect_b32 s26, s34, 0
	s_lshl_b32 s34, s26, 14
	s_addk_i32 s34, 0xc000
	s_cmp_lg_u32 s26, 0
	s_cselect_b32 s26, s34, 0x8000
	v_add_u32_e32 v120, s26, v202
	ds_read_b64_tr_b16 v[112:113], v120 offset:0
	ds_read_b64_tr_b16 v[114:115], v120 offset:0x800
	ds_read_b64_tr_b16 v[116:117], v120 offset:0x200
	ds_read_b64_tr_b16 v[118:119], v120 offset:0xa00
	ds_read_b64_tr_b16 v[124:125], v120 offset:0x400
	ds_read_b64_tr_b16 v[126:127], v120 offset:0xc00
	ds_read_b64_tr_b16 v[128:129], v120 offset:0x600
	ds_read_b64_tr_b16 v[130:131], v120 offset:0xe00
	v_xor_b32_e32 v80, 0x80000000, v203
	v_mov_b32_e32 v81, v80
	v_mov_b32_e32 v82, v80
	v_mov_b32_e32 v83, v80
	v_mov_b32_e32 v84, v80
	v_mov_b32_e32 v85, v80
	v_mov_b32_e32 v86, v80
	v_mov_b32_e32 v87, v80
	v_mov_b32_e32 v88, v80
	v_mov_b32_e32 v89, v80
	v_mov_b32_e32 v90, v80
	v_mov_b32_e32 v91, v80
	v_mov_b32_e32 v92, v80
	v_mov_b32_e32 v93, v80
	v_mov_b32_e32 v94, v80
	v_mov_b32_e32 v95, v80
	s_waitcnt lgkmcnt(6)
	v_mfma_f32_32x32x16_bf16 v[64:79], v[108:111], v[112:115], v[64:79]
	ds_read_b64_tr_b16 v[80:81], v120 offset:0x1000
	ds_read_b64_tr_b16 v[82:83], v120 offset:0x1800
	s_waitcnt lgkmcnt(6)
	v_mfma_f32_32x32x16_bf16 v[48:63], v[108:111], v[116:119], v[48:63]
	ds_read_b64_tr_b16 v[84:85], v120 offset:0x1200
	ds_read_b64_tr_b16 v[86:87], v120 offset:0x1a00
	s_waitcnt lgkmcnt(6)
	v_mfma_f32_32x32x16_bf16 v[32:47], v[108:111], v[124:127], v[32:47]
	ds_read_b64_tr_b16 v[88:89], v120 offset:0x1400
	ds_read_b64_tr_b16 v[90:91], v120 offset:0x1c00
	s_waitcnt lgkmcnt(6)
	v_mfma_f32_32x32x16_bf16 v[16:31], v[108:111], v[128:131], v[16:31]
	ds_read_b64_tr_b16 v[92:93], v120 offset:0x1600
	ds_read_b64_tr_b16 v[94:95], v120 offset:0x1e00
	s_waitcnt lgkmcnt(6)
	v_mfma_f32_32x32x16_bf16 v[64:79], v[104:107], v[80:83], v[64:79]
	ds_read_b64_tr_b16 v[80:81], v120 offset:0x2000
	ds_read_b64_tr_b16 v[82:83], v120 offset:0x2800
	s_waitcnt lgkmcnt(6)
	v_mfma_f32_32x32x16_bf16 v[48:63], v[104:107], v[84:87], v[48:63]
	ds_read_b64_tr_b16 v[84:85], v120 offset:0x2200
	ds_read_b64_tr_b16 v[86:87], v120 offset:0x2a00
	s_waitcnt lgkmcnt(6)
	v_mfma_f32_32x32x16_bf16 v[32:47], v[104:107], v[88:91], v[32:47]
	ds_read_b64_tr_b16 v[88:89], v120 offset:0x2400
	ds_read_b64_tr_b16 v[90:91], v120 offset:0x2c00
	s_waitcnt lgkmcnt(6)
	v_mfma_f32_32x32x16_bf16 v[16:31], v[104:107], v[92:95], v[16:31]
	ds_read_b64_tr_b16 v[92:93], v120 offset:0x2600
	ds_read_b64_tr_b16 v[94:95], v120 offset:0x2e00
	s_waitcnt lgkmcnt(6)
	v_mfma_f32_32x32x16_bf16 v[64:79], v[100:103], v[80:83], v[64:79]
	ds_read_b64_tr_b16 v[80:81], v120 offset:0x3000
	ds_read_b64_tr_b16 v[82:83], v120 offset:0x3800
	s_waitcnt lgkmcnt(6)
	v_mfma_f32_32x32x16_bf16 v[48:63], v[100:103], v[84:87], v[48:63]
	ds_read_b64_tr_b16 v[84:85], v120 offset:0x3200
	ds_read_b64_tr_b16 v[86:87], v120 offset:0x3a00
	s_waitcnt lgkmcnt(6)
	v_mfma_f32_32x32x16_bf16 v[32:47], v[100:103], v[88:91], v[32:47]
	ds_read_b64_tr_b16 v[88:89], v120 offset:0x3400
	ds_read_b64_tr_b16 v[90:91], v120 offset:0x3c00
	s_waitcnt lgkmcnt(6)
	v_mfma_f32_32x32x16_bf16 v[16:31], v[100:103], v[92:95], v[16:31]
	ds_read_b64_tr_b16 v[92:93], v120 offset:0x3600
	ds_read_b64_tr_b16 v[94:95], v120 offset:0x3e00
	s_waitcnt lgkmcnt(6)
	v_mfma_f32_32x32x16_bf16 v[64:79], v[96:99], v[80:83], v[64:79]
	s_waitcnt lgkmcnt(4)
	v_mfma_f32_32x32x16_bf16 v[48:63], v[96:99], v[84:87], v[48:63]
	s_waitcnt lgkmcnt(2)
	v_mfma_f32_32x32x16_bf16 v[32:47], v[96:99], v[88:91], v[32:47]
	s_waitcnt lgkmcnt(0)
	v_mfma_f32_32x32x16_bf16 v[16:31], v[96:99], v[92:95], v[16:31]
	s_waitcnt lgkmcnt(0)
	s_barrier
	s_andn2_b64 vcc, exec, s[38:39]
	s_cbranch_vccz .LBB0_633
	s_and_saveexec_b64 s[34:35], s[10:11]
	s_cbranch_execz .LBB0_593
	s_branch .LBB0_634

; #define SBAR() __builtin_amdgcn_sched_barrier(0)
; __device__ __forceinline__ int kg(int row) { return (row >> 1) & 7; }
; __device__ __forceinline__ int v_rd_base(int lane) { return ((lane & 3) << 3) | (((lane >> 2) & 3) << 6) | (((lane >> 4) & 1) << 5) | (((lane >> 5) & 1) << 8); }
; #define BAR_ALL() asm volatile("s_waitcnt lgkmcnt(0)\n\ts_barrier" ::: "memory")
; #define LWN1(a) do { if constexpr (NW == 0) LW1(0, a); else if constexpr (NW == 1) LW1(1, a); else if constexpr (NW == 2) LW1(2, a); else if constexpr (NW == 3) LW1(3, a); else if constexpr (NW == 4) LW1(4, a); else if constexpr (NW == 5) LW1(5, a); else LW1(6, a); } while (0)
; #define DMA_K(tile, b) DMA_KP(Kh, tile, b)
; #define DMA_V(tile, b) DMA_VP(Vh, tile, b)
; template <int DQK, bool HASQK, bool HASPV, int J> ...
;     ...
;     if constexpr (J < NS) {
;         constexpr int rd1 = (J + 1 < NS) ? ((J + 1 < NQS) ? 1 : 2) : 0, rd2 = (J + 2 < NS) ? ((J + 2 < NQS) ? 1 : 2) : 0, rd3 = (J + 3 < NS) ? ((J + 3 < NQS) ? 1 : 2) : 0, NW = rd1 + rd2 + rd3;
;     ...
;         if constexpr (J < NQS) { constexpr int d0 = J >> 1, h = J & 1;
;             LWN1(kf[d0][h]); SBAR();
;             if constexpr (h == 0) p0 = __builtin_amdgcn_mfma_f32_32x32x16_bf16(kf[d0][0], qr[d0], (d0 == 0) ? negm : p0, 0, 0, 0);
;             else p1 = __builtin_amdgcn_mfma_f32_32x32x16_bf16(kf[d0][1], qr[d0], (d0 == 0) ? negm : p1, 0, 0, 0);
;         } else { constexpr int q = J - NQS, g = q >> 2, d = q & 3;
;             LWN2(vf[g][2 * d], vf[g][2 * d + 1]); SBAR();
;             o[d] = __builtin_amdgcn_mfma_f32_32x32x16_bf16(pa[g], (bf16x8){vf[g][2 * d][0], vf[g][2 * d][1], vf[g][2 * d][2], vf[g][2 * d][3], vf[g][2 * d + 1][0], vf[g][2 * d + 1][1], vf[g][2 * d + 1][2], vf[g][2 * d + 1][3]}, o[d], 0, 0, 0);
;         }
;     ...
;     const int vb0 = (int)(uintptr_t)V_lds + v_rd_base(lane);
;     int ka[4];
; #pragma unroll
;     for (int b = 0; b < 4; ++b) ka[b] = (int)(uintptr_t)lds + r32 * RB + ((b * 32 + hi * 16) ^ (kg(r32) << 4));
;     f32x16 p0, p1; bf16x8 pa0, pa1, pa2, pa3;
;     asm volatile("s_waitcnt vmcnt(0)" ::: "memory"); BAR_ALL();
;     if (ATT_SKEW && g == 1) BAR_ALL();
;     ...
;     int ci = 0;
;     if (DMA_M) { DMA_K(2, 2); DMA_V(1, 1); }
;     SEG_M(true, false, 0, 0); BAR_ALL();
.LBB0_648:
	v_lshlrev_b32_e32 v26, 3, v156
	v_and_b32_e32 v23, 0xc0, v23
	s_cmp_lg_u32 0, -1
	v_and_or_b32 v23, v26, 24, v23
	v_and_b32_e32 v24, 32, v24
	v_and_b32_e32 v27, 0x100, v26
	s_cselect_b32 s10, 0, 0
	v_lshlrev_b32_e32 v154, 4, v25
	v_or3_b32 v23, v23, v24, v27
	v_lshl_add_u32 v24, v22, 7, s10
	v_and_b32_e32 v25, 0x70, v26
	v_add_u32_e32 v26, 32, v154
	v_xad_u32 v143, v26, v25, v24
	v_add_u32_e32 v26, 64, v154
	v_xad_u32 v160, v26, v25, v24
	v_add_u32_e32 v26, 0x60, v154
	v_xad_u32 v141, v154, v25, v24
	v_xad_u32 v161, v26, v25, v24
	s_addk_i32 s10, 0x6000
	ds_read_b128 v[24:27], v141 offset:0
	ds_read_b128 v[28:31], v141 offset:0x1000
	ds_read_b128 v[32:35], v143 offset:0
	ds_read_b128 v[36:39], v143 offset:0x1000
	v_add_u32_e32 v157, s10, v23
	v_cndmask_b32_e64 v23, 0, 1, s[26:27]
	s_mov_b32 s86, 0
	v_lshlrev_b32_e32 v23, 7, v23
	v_mov_b64_e32 v[94:95], v[14:15]
	v_mov_b64_e32 v[92:93], v[12:13]
	v_mov_b64_e32 v[90:91], v[10:11]
	v_mov_b64_e32 v[88:89], v[8:9]
	v_mov_b64_e32 v[86:87], v[6:7]
	v_mov_b64_e32 v[84:85], v[4:5]
	v_mov_b64_e32 v[82:83], v[2:3]
	v_mov_b64_e32 v[80:81], v[0:1]
	s_waitcnt lgkmcnt(3)
	s_waitcnt vmcnt(0)
	s_nop 0
	v_mfma_f32_32x32x16_bf16 v[96:111], v[24:27], v[112:115], v[80:95]
	ds_read_b128 v[24:27], v160 offset:0
	s_waitcnt lgkmcnt(3)
	v_mfma_f32_32x32x16_bf16 v[80:95], v[28:31], v[112:115], v[80:95]
	ds_read_b128 v[28:31], v160 offset:0x1000
	s_waitcnt lgkmcnt(3)
	v_mfma_f32_32x32x16_bf16 v[96:111], v[32:35], v[116:119], v[96:111]
	ds_read_b128 v[32:35], v161 offset:0
	s_waitcnt lgkmcnt(3)
	v_mfma_f32_32x32x16_bf16 v[80:95], v[36:39], v[116:119], v[80:95]
	ds_read_b128 v[36:39], v161 offset:0x1000
	s_waitcnt lgkmcnt(3)
	v_mfma_f32_32x32x16_bf16 v[96:111], v[24:27], v[120:123], v[96:111]
	s_waitcnt lgkmcnt(2)
	v_mfma_f32_32x32x16_bf16 v[80:95], v[28:31], v[120:123], v[80:95]
	s_waitcnt lgkmcnt(1)
	v_mfma_f32_32x32x16_bf16 v[96:111], v[32:35], v[124:127], v[96:111]
	s_waitcnt lgkmcnt(0)
	v_mfma_f32_32x32x16_bf16 v[80:95], v[36:39], v[124:127], v[80:95]
	s_and_b32 s46, s46, 3
	s_lshl_b64 s[44:45], s[44:45], 23
	s_lshl_b32 s46, s46, 8
	v_lshlrev_b32_e32 v20, 2, v20
	v_lshlrev_b32_e32 v17, 2, v17
	s_or_b32 s44, s44, s46
	v_and_b32_e32 v20, 0xffffe000, v20
	v_lshlrev_b32_e32 v18, 10, v18
	v_and_b32_e32 v17, 0xffffe000, v17
	v_lshl_add_u32 v155, v22, 2, s67
	v_or_b32_e32 v22, s44, v23
	v_mov_b32_e32 v23, s45
	v_or3_b32 v20, v20, v18, v21
	s_add_u32 s44, s73, s44
	v_or3_b32 v17, v17, v18, v19
	s_waitcnt lgkmcnt(0)
	s_barrier
	v_lshl_add_u64 v[22:23], s[24:25], 0, v[22:23]
	v_add_u32_e32 v20, v20, v16
	v_mov_b32_e32 v21, v139
	s_addc_u32 s45, s74, s45
	v_add_u32_e32 v16, v17, v16
	v_mov_b32_e32 v17, v139
	v_mov_b32_e32 v64, v139
	v_mov_b32_e32 v65, v139
	v_lshl_add_u64 v[144:145], v[22:23], 0, v[138:139]
	v_lshl_add_u64 v[146:147], s[44:45], 0, v[20:21]
	v_lshl_add_u64 v[148:149], s[44:45], 0, v[16:17]
	v_mov_b32_e32 v66, v139
	v_mov_b32_e32 v67, v139
	v_mov_b32_e32 v68, v139
	v_mov_b32_e32 v69, v139
	v_mov_b32_e32 v70, v139
	v_mov_b32_e32 v71, v139
	v_mov_b32_e32 v72, v139
	v_mov_b32_e32 v73, v139
	v_mov_b32_e32 v74, v139
	v_mov_b32_e32 v75, v139
	v_mov_b32_e32 v76, v139
	v_mov_b32_e32 v77, v139
	v_mov_b32_e32 v78, v139
	v_mov_b32_e32 v79, v139
	v_mov_b64_e32 v[48:49], v[64:65]
	v_mov_b64_e32 v[32:33], v[64:65]
	v_mov_b64_e32 v[16:17], v[64:65]
	v_cmp_gt_u32_e64 s[10:11], 32, v156
	v_mov_b32_e32 v159, 0
	s_mov_b64 s[44:45], 0
	v_mov_b64_e32 v[50:51], v[66:67]
	v_mov_b64_e32 v[52:53], v[68:69]
	v_mov_b64_e32 v[54:55], v[70:71]
	v_mov_b64_e32 v[56:57], v[72:73]
	v_mov_b64_e32 v[58:59], v[74:75]
	v_mov_b64_e32 v[60:61], v[76:77]
	v_mov_b64_e32 v[62:63], v[78:79]
	v_mov_b64_e32 v[34:35], v[66:67]
	v_mov_b64_e32 v[36:37], v[68:69]
	v_mov_b64_e32 v[38:39], v[70:71]
	v_mov_b64_e32 v[40:41], v[72:73]
	v_mov_b64_e32 v[42:43], v[74:75]
	v_mov_b64_e32 v[44:45], v[76:77]
	v_mov_b64_e32 v[46:47], v[78:79]
	v_mov_b64_e32 v[18:19], v[66:67]
	v_mov_b64_e32 v[20:21], v[68:69]
	v_mov_b64_e32 v[22:23], v[70:71]
	v_mov_b64_e32 v[24:25], v[72:73]
	v_mov_b64_e32 v[26:27], v[74:75]
	v_mov_b64_e32 v[28:29], v[76:77]
	v_mov_b64_e32 v[30:31], v[78:79]
	v_mov_b32_e32 v158, 0
	s_branch .LBB0_652

; #define PK4(P, BASE, OUT) do { u32x4 w = {cvtpk(P[BASE + 0], P[BASE + 1]), cvtpk(P[BASE + 2], P[BASE + 3]), cvtpk(P[BASE + 4], P[BASE + 5]), cvtpk(P[BASE + 6], P[BASE + 7])}; \
;     OUT = *reinterpret_cast<bf16x8*>(&w); } while (0)
; __device__ __forceinline__ void smax_tile(f32x16& p0, f32x16& p1, float& mhat, float& l_reg, f32x16 (&o)[4], float* al_l, const bool first, int r32, int hi,
;                                           bf16x8& pa0, bf16x8& pa1, bf16x8& pa2, bf16x8& pa3) {
;     ...
; #pragma unroll
;     for (int r = 0; r < 16; ++r) p0[r] = __builtin_amdgcn_exp2f(p0[r]);
; #pragma unroll
;     for (int r = 0; r < 16; ++r) p1[r] = __builtin_amdgcn_exp2f(p1[r]);
;     float ps = p0[0];
; #pragma unroll
;     for (int r = 1; r < 16; ++r) ps += p0[r];
; #pragma unroll
;     for (int r = 0; r < 16; ++r) ps += p1[r];
;     { auto rr = __builtin_amdgcn_permlane32_swap(__float_as_uint(ps), __float_as_uint(ps), false, false); ps = __uint_as_float(rr[0]) + __uint_as_float(rr[1]); }
;     l_reg += ps;
;     ...
;     PK4(p0, 0, pa0); PK4(p0, 8, pa1); PK4(p1, 0, pa2); PK4(p1, 8, pa3);
.LBB0_651:
	v_exp_f32_e32 v96, v96
	v_exp_f32_e32 v97, v97
	v_exp_f32_e32 v98, v98
	v_exp_f32_e32 v99, v99
	v_exp_f32_e32 v100, v100
	v_exp_f32_e32 v101, v101
	v_add_f32_e32 v128, v96, v97
	v_exp_f32_e32 v102, v102
	v_add_f32_e32 v128, v98, v128
	v_exp_f32_e32 v103, v103
	v_add_f32_e32 v128, v99, v128
	v_exp_f32_e32 v104, v104
	v_add_f32_e32 v128, v100, v128
	v_exp_f32_e32 v105, v105
	v_add_f32_e32 v128, v101, v128
	v_exp_f32_e32 v106, v106
	v_add_f32_e32 v128, v102, v128
	v_exp_f32_e32 v107, v107
	v_add_f32_e32 v128, v103, v128
	v_exp_f32_e32 v108, v108
	v_add_f32_e32 v128, v104, v128
	v_exp_f32_e32 v109, v109
	v_add_f32_e32 v128, v105, v128
	v_exp_f32_e32 v110, v110
	v_add_f32_e32 v128, v106, v128
	v_exp_f32_e32 v111, v111
	v_add_f32_e32 v128, v107, v128
	v_exp_f32_e32 v80, v80
	v_add_f32_e32 v128, v108, v128
	v_exp_f32_e32 v81, v81
	v_add_f32_e32 v128, v109, v128
	v_exp_f32_e32 v82, v82
	v_add_f32_e32 v128, v110, v128
	v_exp_f32_e32 v83, v83
	v_add_f32_e32 v128, v111, v128
	v_exp_f32_e32 v84, v84
	v_add_f32_e32 v128, v80, v128
	v_exp_f32_e32 v85, v85
	v_add_f32_e32 v128, v81, v128
	v_exp_f32_e32 v86, v86
	v_add_f32_e32 v128, v82, v128
	v_exp_f32_e32 v87, v87
	v_add_f32_e32 v128, v83, v128
	v_exp_f32_e32 v88, v88
	v_add_f32_e32 v128, v84, v128
	v_exp_f32_e32 v89, v89
	v_add_f32_e32 v128, v85, v128
	v_exp_f32_e32 v90, v90
	v_add_f32_e32 v128, v86, v128
	v_exp_f32_e32 v91, v91
	v_add_f32_e32 v128, v87, v128
	v_exp_f32_e32 v92, v92
	v_add_f32_e32 v128, v88, v128
	v_exp_f32_e32 v93, v93
	v_add_f32_e32 v128, v89, v128
	v_exp_f32_e32 v94, v94
	v_add_f32_e32 v128, v90, v128
	v_exp_f32_e32 v95, v95
	v_add_f32_e32 v128, v91, v128
	v_add_f32_e32 v128, v92, v128
	v_add_f32_e32 v128, v93, v128
	v_add_f32_e32 v128, v94, v128
	v_add_f32_e32 v128, v95, v128
	v_mov_b32_e32 v129, v128
	v_cvt_pk_bf16_f32 v162, v96, v97
	v_cvt_pk_bf16_f32 v163, v98, v99
	v_permlane32_swap_b32_e32 v128, v129
	v_add_f32_e32 v128, v128, v129
	v_add_f32_e32 v159, v159, v128
	v_cvt_pk_bf16_f32 v164, v100, v101
	v_cvt_pk_bf16_f32 v165, v102, v103
	v_cvt_pk_bf16_f32 v166, v104, v105
	v_cvt_pk_bf16_f32 v167, v106, v107
	v_cvt_pk_bf16_f32 v168, v108, v109
	v_cvt_pk_bf16_f32 v169, v110, v111
	v_cvt_pk_bf16_f32 v132, v80, v81
	v_cvt_pk_bf16_f32 v133, v82, v83
	v_cvt_pk_bf16_f32 v134, v84, v85
	v_cvt_pk_bf16_f32 v135, v86, v87
	v_cvt_pk_bf16_f32 v128, v88, v89
	v_cvt_pk_bf16_f32 v129, v90, v91
	v_cvt_pk_bf16_f32 v130, v92, v93
	v_cvt_pk_bf16_f32 v131, v94, v95
	s_cmp_lg_u32 s86, 0
	s_waitcnt lgkmcnt(0)
	s_barrier
; #define SBAR() __builtin_amdgcn_sched_barrier(0)
; #define LWN1(a) do { if constexpr (NW == 0) LW1(0, a); else if constexpr (NW == 1) LW1(1, a); else if constexpr (NW == 2) LW1(2, a); else if constexpr (NW == 3) LW1(3, a); else if constexpr (NW == 4) LW1(4, a); else if constexpr (NW == 5) LW1(5, a); else LW1(6, a); } while (0)
; #define LWN2(a, b) do { if constexpr (NW == 0) LW2(0, a, b); else if constexpr (NW == 1) LW2(1, a, b); else if constexpr (NW == 2) LW2(2, a, b); else if constexpr (NW == 3) LW2(3, a, b); else if constexpr (NW == 4) LW2(4, a, b); else if constexpr (NW == 5) LW2(5, a, b); else LW2(6, a, b); } while (0)
; template <int DQK, bool HASQK, bool HASPV, int J> ...
;     constexpr int NQS = HASQK ? 2 * (DQK / 16) : 0, NS = NQS + (HASPV ? 16 : 0);
;     if constexpr (J < NS) {
;         constexpr int rd1 = (J + 1 < NS) ? ((J + 1 < NQS) ? 1 : 2) : 0, rd2 = (J + 2 < NS) ? ((J + 2 < NQS) ? 1 : 2) : 0, rd3 = (J + 3 < NS) ? ((J + 3 < NQS) ? 1 : 2) : 0, NW = rd1 + rd2 + rd3;
;     ...
;         if constexpr (J < NQS) { constexpr int d0 = J >> 1, h = J & 1;
;             LWN1(kf[d0][h]); SBAR();
;             if constexpr (h == 0) p0 = __builtin_amdgcn_mfma_f32_32x32x16_bf16(kf[d0][0], qr[d0], (d0 == 0) ? negm : p0, 0, 0, 0);
;             else p1 = __builtin_amdgcn_mfma_f32_32x32x16_bf16(kf[d0][1], qr[d0], (d0 == 0) ? negm : p1, 0, 0, 0);
;         } else { constexpr int q = J - NQS, g = q >> 2, d = q & 3;
;             LWN2(vf[g][2 * d], vf[g][2 * d + 1]); SBAR();
;             o[d] = __builtin_amdgcn_mfma_f32_32x32x16_bf16(pa[g], (bf16x8){vf[g][2 * d][0], vf[g][2 * d][1], vf[g][2 * d][2], vf[g][2 * d][3], vf[g][2 * d + 1][0], vf[g][2 * d + 1][1], vf[g][2 * d + 1][2], vf[g][2 * d + 1][3]}, o[d], 0, 0, 0);
;         }
;     ...
;         SBAR();
;         slot_read<DQK, HASQK, HASPV, J + 4>(kf, vf, ka_, vb_);
;         SBAR();
;         slot_run<DQK, HASQK, HASPV, J + 1>(kf, vf, ka_, vb_, qr, p0, p1, negm, o, pa);
	s_cselect_b32 s46, s87, 0x8000
	s_lshl_b32 s47, s86, 13
	v_add_u32_e32 v81, s47, v141
	v_add_u32_e32 v82, s47, v143
	ds_read_b128 v[170:173], v81 offset:0
	ds_read_b128 v[174:177], v81 offset:0x1000
	ds_read_b128 v[178:181], v82 offset:0
	ds_read_b128 v[182:185], v82 offset:0x1000
	v_xor_b32_e32 v80, 0x80000000, v158
	v_add_u32_e32 v186, s47, v160
	v_add_u32_e32 v187, s47, v161
	v_add_u32_e32 v188, s46, v157
	v_mov_b32_e32 v81, v80
	v_mov_b32_e32 v82, v80
	v_mov_b32_e32 v83, v80
	v_mov_b32_e32 v84, v80
	v_mov_b32_e32 v85, v80
	v_mov_b32_e32 v86, v80
	v_mov_b32_e32 v87, v80
	v_mov_b32_e32 v88, v80
	v_mov_b32_e32 v89, v80
	v_mov_b32_e32 v90, v80
	v_mov_b32_e32 v91, v80
	v_mov_b32_e32 v92, v80
	v_mov_b32_e32 v93, v80
	v_mov_b32_e32 v94, v80
	v_mov_b32_e32 v95, v80
	s_waitcnt lgkmcnt(3)
	s_nop 1
	v_mfma_f32_32x32x16_bf16 v[96:111], v[170:173], v[112:115], v[80:95]
	ds_read_b128 v[170:173], v186 offset:0
	s_waitcnt lgkmcnt(3)
	v_mfma_f32_32x32x16_bf16 v[80:95], v[174:177], v[112:115], v[80:95]
	ds_read_b128 v[174:177], v186 offset:0x1000
	s_waitcnt lgkmcnt(3)
	v_mfma_f32_32x32x16_bf16 v[96:111], v[178:181], v[116:119], v[96:111]
	ds_read_b128 v[178:181], v187 offset:0
	s_waitcnt lgkmcnt(3)
	v_mfma_f32_32x32x16_bf16 v[80:95], v[182:185], v[116:119], v[80:95]
	ds_read_b128 v[182:185], v187 offset:0x1000
	s_waitcnt lgkmcnt(3)
	v_mfma_f32_32x32x16_bf16 v[96:111], v[170:173], v[120:123], v[96:111]
	ds_read_b64_tr_b16 v[170:171], v188 offset:0
	ds_read_b64_tr_b16 v[172:173], v188 offset:0x800
	s_waitcnt lgkmcnt(4)
	v_mfma_f32_32x32x16_bf16 v[80:95], v[174:177], v[120:123], v[80:95]
	ds_read_b64_tr_b16 v[174:175], v188 offset:0x200
	ds_read_b64_tr_b16 v[176:177], v188 offset:0xa00
	s_waitcnt lgkmcnt(5)
	v_mfma_f32_32x32x16_bf16 v[96:111], v[178:181], v[124:127], v[96:111]
	ds_read_b64_tr_b16 v[178:179], v188 offset:0x400
	ds_read_b64_tr_b16 v[180:181], v188 offset:0xc00
	s_waitcnt lgkmcnt(6)
	v_mfma_f32_32x32x16_bf16 v[80:95], v[182:185], v[124:127], v[80:95]
	ds_read_b64_tr_b16 v[182:183], v188 offset:0x600
	ds_read_b64_tr_b16 v[184:185], v188 offset:0xe00
	s_waitcnt lgkmcnt(6)
	v_mfma_f32_32x32x16_bf16 v[64:79], v[162:165], v[170:173], v[64:79]
	ds_read_b64_tr_b16 v[170:171], v188 offset:0x1000
	ds_read_b64_tr_b16 v[172:173], v188 offset:0x1800
	s_waitcnt lgkmcnt(6)
	v_mfma_f32_32x32x16_bf16 v[48:63], v[162:165], v[174:177], v[48:63]
	ds_read_b64_tr_b16 v[174:175], v188 offset:0x1200
	ds_read_b64_tr_b16 v[176:177], v188 offset:0x1a00
	s_waitcnt lgkmcnt(6)
	v_mfma_f32_32x32x16_bf16 v[32:47], v[162:165], v[178:181], v[32:47]
	ds_read_b64_tr_b16 v[178:179], v188 offset:0x1400
	ds_read_b64_tr_b16 v[180:181], v188 offset:0x1c00
	s_waitcnt lgkmcnt(6)
	v_mfma_f32_32x32x16_bf16 v[16:31], v[162:165], v[182:185], v[16:31]
	ds_read_b64_tr_b16 v[162:163], v188 offset:0x1600
	ds_read_b64_tr_b16 v[164:165], v188 offset:0x1e00
	s_waitcnt lgkmcnt(6)
	v_mfma_f32_32x32x16_bf16 v[64:79], v[166:169], v[170:173], v[64:79]
	ds_read_b64_tr_b16 v[170:171], v188 offset:0x2000
	ds_read_b64_tr_b16 v[172:173], v188 offset:0x2800
	s_waitcnt lgkmcnt(6)
	v_mfma_f32_32x32x16_bf16 v[48:63], v[166:169], v[174:177], v[48:63]
	ds_read_b64_tr_b16 v[174:175], v188 offset:0x2200
	ds_read_b64_tr_b16 v[176:177], v188 offset:0x2a00
	s_waitcnt lgkmcnt(6)
	v_mfma_f32_32x32x16_bf16 v[32:47], v[166:169], v[178:181], v[32:47]
	ds_read_b64_tr_b16 v[178:179], v188 offset:0x2400
	ds_read_b64_tr_b16 v[180:181], v188 offset:0x2c00
	s_waitcnt lgkmcnt(6)
	v_mfma_f32_32x32x16_bf16 v[16:31], v[166:169], v[162:165], v[16:31]
	ds_read_b64_tr_b16 v[162:163], v188 offset:0x2600
	ds_read_b64_tr_b16 v[164:165], v188 offset:0x2e00
	s_waitcnt lgkmcnt(6)
	v_mfma_f32_32x32x16_bf16 v[64:79], v[132:135], v[170:173], v[64:79]
	ds_read_b64_tr_b16 v[166:167], v188 offset:0x3000
	ds_read_b64_tr_b16 v[168:169], v188 offset:0x3800
	s_waitcnt lgkmcnt(6)
	v_mfma_f32_32x32x16_bf16 v[48:63], v[132:135], v[174:177], v[48:63]
	ds_read_b64_tr_b16 v[170:171], v188 offset:0x3200
	ds_read_b64_tr_b16 v[172:173], v188 offset:0x3a00
	s_waitcnt lgkmcnt(6)
	v_mfma_f32_32x32x16_bf16 v[32:47], v[132:135], v[178:181], v[32:47]
	ds_read_b64_tr_b16 v[174:175], v188 offset:0x3400
	ds_read_b64_tr_b16 v[176:177], v188 offset:0x3c00
	s_waitcnt lgkmcnt(6)
	v_mfma_f32_32x32x16_bf16 v[16:31], v[132:135], v[162:165], v[16:31]
	ds_read_b64_tr_b16 v[132:133], v188 offset:0x3600
	ds_read_b64_tr_b16 v[134:135], v188 offset:0x3e00
	s_waitcnt lgkmcnt(6)
	v_mfma_f32_32x32x16_bf16 v[64:79], v[128:131], v[166:169], v[64:79]
	s_waitcnt lgkmcnt(4)
	v_mfma_f32_32x32x16_bf16 v[48:63], v[128:131], v[170:173], v[48:63]
	s_waitcnt lgkmcnt(2)
	v_mfma_f32_32x32x16_bf16 v[32:47], v[128:131], v[174:177], v[32:47]
	s_waitcnt lgkmcnt(0)
	v_mfma_f32_32x32x16_bf16 v[16:31], v[128:131], v[132:135], v[16:31]
	v_lshl_add_u64 v[144:145], v[144:145], 0, s[28:29]
	v_lshl_add_u64 v[146:147], v[146:147], 0, s[28:29]
	v_lshl_add_u64 v[148:149], v[148:149], 0, s[28:29]
	s_waitcnt vmcnt(0)
	s_add_u32 s44, s44, 0x10000
	s_waitcnt lgkmcnt(0)
	s_barrier
	s_addc_u32 s45, s45, 0
	s_cmp_eq_u32 s44, 0x7f0000
	s_cbranch_scc1 .LBB0_662

; #define SBAR() __builtin_amdgcn_sched_barrier(0)
; template <int DQK, bool HASQK, bool HASPV, int J>
; __device__ __forceinline__ void slot_read(bf16x8 (&kf)[DQK / 16][2], s16x4 (&vf)[4][8], const int (&ka_)[4], int vb_) {
;     constexpr int NQS = HASQK ? 2 * (DQK / 16) : 0, NS = NQS + (HASPV ? 16 : 0);
;     if constexpr (J < NQS) { constexpr int d0 = J >> 1, h = J & 1; dsr128<(d0 >> 2) * 128 + h * 32 * DQK * 2>(kf[d0][h], ka_[d0 & 3]); }
;     else if constexpr (J < NS) { constexpr int q = J - NQS, g = q >> 2, d = q & 3; dstr64<v_rd_off(d, g, 0)>(vf[g][2 * d], vb_); dstr64<v_rd_off(d, g, 1)>(vf[g][2 * d + 1], vb_); }
; }
; template <int DQK, bool HASQK, bool HASPV, int J> ...
;     constexpr int NQS = HASQK ? 2 * (DQK / 16) : 0, NS = NQS + (HASPV ? 16 : 0);
;     if constexpr (J < NS) {
;         constexpr int rd1 = (J + 1 < NS) ? ((J + 1 < NQS) ? 1 : 2) : 0, rd2 = (J + 2 < NS) ? ((J + 2 < NQS) ? 1 : 2) : 0, rd3 = (J + 3 < NS) ? ((J + 3 < NQS) ? 1 : 2) : 0, NW = rd1 + rd2 + rd3;
;     ...
;         if constexpr (J < NQS) { constexpr int d0 = J >> 1, h = J & 1;
;             LWN1(kf[d0][h]); SBAR();
;             if constexpr (h == 0) p0 = __builtin_amdgcn_mfma_f32_32x32x16_bf16(kf[d0][0], qr[d0], (d0 == 0) ? negm : p0, 0, 0, 0);
;             else p1 = __builtin_amdgcn_mfma_f32_32x32x16_bf16(kf[d0][1], qr[d0], (d0 == 0) ? negm : p1, 0, 0, 0);
;         } else { constexpr int q = J - NQS, g = q >> 2, d = q & 3;
;             LWN2(vf[g][2 * d], vf[g][2 * d + 1]); SBAR();
;             o[d] = __builtin_amdgcn_mfma_f32_32x32x16_bf16(pa[g], (bf16x8){vf[g][2 * d][0], vf[g][2 * d][1], vf[g][2 * d][2], vf[g][2 * d][3], vf[g][2 * d + 1][0], vf[g][2 * d + 1][1], vf[g][2 * d + 1][2], vf[g][2 * d + 1][3]}, o[d], 0, 0, 0);
;         }
;     ...
;         SBAR();
;         slot_read<DQK, HASQK, HASPV, J + 4>(kf, vf, ka_, vb_);
;         SBAR();
;         slot_run<DQK, HASQK, HASPV, J + 1>(kf, vf, ka_, vb_, qr, p0, p1, negm, o, pa);
;     }
; }
; template <int DQK, bool HASQK, bool HASPV>
; __device__ __forceinline__ void seg_m2(const int (&ka_)[4], int vb_, const bf16x8* qr, f32x16& p0, f32x16& p1, const float nm, f32x16 (&o)[4], bf16x8 pa0, bf16x8 pa1, bf16x8 pa2, bf16x8 pa3) {
;     bf16x8 kf[DQK / 16][2]; s16x4 vf[4][8]; const bf16x8 pa[4] = {pa0, pa1, pa2, pa3};
.LBB0_671:
	s_add_i32 s36, s86, 1
	s_cmp_lg_u32 s86, 2
	s_cselect_b32 s36, s36, 0
	s_lshl_b32 s37, s36, 14
	s_addk_i32 s37, 0xc000
	s_cmp_lg_u32 s36, 0
	s_cselect_b32 s36, s37, 0x8000
	v_add_u32_e32 v121, s36, v157
	ds_read_b64_tr_b16 v[112:113], v121 offset:0
	ds_read_b64_tr_b16 v[114:115], v121 offset:0x800
	ds_read_b64_tr_b16 v[116:117], v121 offset:0x200
	ds_read_b64_tr_b16 v[118:119], v121 offset:0xa00
	ds_read_b64_tr_b16 v[122:123], v121 offset:0x400
	ds_read_b64_tr_b16 v[124:125], v121 offset:0xc00
	ds_read_b64_tr_b16 v[126:127], v121 offset:0x600
	ds_read_b64_tr_b16 v[128:129], v121 offset:0xe00
	v_xor_b32_e32 v80, 0x80000000, v158
	v_mov_b32_e32 v81, v80
	v_mov_b32_e32 v82, v80
	v_mov_b32_e32 v83, v80
	v_mov_b32_e32 v84, v80
	v_mov_b32_e32 v85, v80
	v_mov_b32_e32 v86, v80
	v_mov_b32_e32 v87, v80
	v_mov_b32_e32 v88, v80
	v_mov_b32_e32 v89, v80
	v_mov_b32_e32 v90, v80
	v_mov_b32_e32 v91, v80
	v_mov_b32_e32 v92, v80
	v_mov_b32_e32 v93, v80
	v_mov_b32_e32 v94, v80
	v_mov_b32_e32 v95, v80
	s_waitcnt lgkmcnt(6)
	v_mfma_f32_32x32x16_bf16 v[64:79], v[108:111], v[112:115], v[64:79]
	ds_read_b64_tr_b16 v[80:81], v121 offset:0x1000
	ds_read_b64_tr_b16 v[82:83], v121 offset:0x1800
	s_waitcnt lgkmcnt(6)
	v_mfma_f32_32x32x16_bf16 v[48:63], v[108:111], v[116:119], v[48:63]
	ds_read_b64_tr_b16 v[84:85], v121 offset:0x1200
	ds_read_b64_tr_b16 v[86:87], v121 offset:0x1a00
	s_waitcnt lgkmcnt(6)
	v_mfma_f32_32x32x16_bf16 v[32:47], v[108:111], v[122:125], v[32:47]
	ds_read_b64_tr_b16 v[88:89], v121 offset:0x1400
	ds_read_b64_tr_b16 v[90:91], v121 offset:0x1c00
	s_waitcnt lgkmcnt(6)
	v_mfma_f32_32x32x16_bf16 v[16:31], v[108:111], v[126:129], v[16:31]
	ds_read_b64_tr_b16 v[92:93], v121 offset:0x1600
	ds_read_b64_tr_b16 v[94:95], v121 offset:0x1e00
	s_waitcnt lgkmcnt(6)
	v_mfma_f32_32x32x16_bf16 v[64:79], v[104:107], v[80:83], v[64:79]
	ds_read_b64_tr_b16 v[80:81], v121 offset:0x2000
	ds_read_b64_tr_b16 v[82:83], v121 offset:0x2800
	s_waitcnt lgkmcnt(6)
	v_mfma_f32_32x32x16_bf16 v[48:63], v[104:107], v[84:87], v[48:63]
	ds_read_b64_tr_b16 v[84:85], v121 offset:0x2200
	ds_read_b64_tr_b16 v[86:87], v121 offset:0x2a00
	s_waitcnt lgkmcnt(6)
	v_mfma_f32_32x32x16_bf16 v[32:47], v[104:107], v[88:91], v[32:47]
	ds_read_b64_tr_b16 v[88:89], v121 offset:0x2400
	ds_read_b64_tr_b16 v[90:91], v121 offset:0x2c00
	s_waitcnt lgkmcnt(6)
	v_mfma_f32_32x32x16_bf16 v[16:31], v[104:107], v[92:95], v[16:31]
	ds_read_b64_tr_b16 v[92:93], v121 offset:0x2600
	ds_read_b64_tr_b16 v[94:95], v121 offset:0x2e00
	s_waitcnt lgkmcnt(6)
	v_mfma_f32_32x32x16_bf16 v[64:79], v[100:103], v[80:83], v[64:79]
	ds_read_b64_tr_b16 v[80:81], v121 offset:0x3000
	ds_read_b64_tr_b16 v[82:83], v121 offset:0x3800
	s_waitcnt lgkmcnt(6)
	v_mfma_f32_32x32x16_bf16 v[48:63], v[100:103], v[84:87], v[48:63]
	ds_read_b64_tr_b16 v[84:85], v121 offset:0x3200
	ds_read_b64_tr_b16 v[86:87], v121 offset:0x3a00
	s_waitcnt lgkmcnt(6)
	v_mfma_f32_32x32x16_bf16 v[32:47], v[100:103], v[88:91], v[32:47]
	ds_read_b64_tr_b16 v[88:89], v121 offset:0x3400
	ds_read_b64_tr_b16 v[90:91], v121 offset:0x3c00
	s_waitcnt lgkmcnt(6)
	v_mfma_f32_32x32x16_bf16 v[16:31], v[100:103], v[92:95], v[16:31]
	ds_read_b64_tr_b16 v[92:93], v121 offset:0x3600
	ds_read_b64_tr_b16 v[94:95], v121 offset:0x3e00
	s_waitcnt lgkmcnt(6)
	v_mfma_f32_32x32x16_bf16 v[64:79], v[96:99], v[80:83], v[64:79]
	s_waitcnt lgkmcnt(4)
	v_mfma_f32_32x32x16_bf16 v[48:63], v[96:99], v[84:87], v[48:63]
	s_waitcnt lgkmcnt(2)
	v_mfma_f32_32x32x16_bf16 v[32:47], v[96:99], v[88:91], v[32:47]
	s_waitcnt lgkmcnt(0)
	v_mfma_f32_32x32x16_bf16 v[16:31], v[96:99], v[92:95], v[16:31]
	s_waitcnt lgkmcnt(0)
	s_barrier
	s_andn2_b64 vcc, exec, s[12:13]
	s_cbranch_vccz .LBB0_676
	s_and_saveexec_b64 s[12:13], s[10:11]
